# GLA prep phase A: four cumulative-sum shuffle tails deferred and interleaved (8 serialized ds_bpermute round trips per iteration -> 2)
# baseline (speedup 1.0000x reference)
.LBB0_1145:
	s_add_i32 s39, s39, 2
	s_cmpk_lt_i32 s39, 0x43
	s_cselect_b64 s[2:3], -1, 0
	s_cmpk_gt_i32 s39, 0x42
	s_waitcnt lgkmcnt(0)
	s_barrier
	s_cselect_b64 s[26:27], -1, 0
	s_and_b64 vcc, exec, s[26:27]
	s_cbranch_vccnz .LBB0_1155
	s_waitcnt vmcnt(36)
	v_mfma_f32_16x16x32_bf16 v[152:155], v[36:39], v[6:9], v[10:13]
	v_add_u32_e32 v138, -16, v213
	v_and_b32_e32 v139, 64, v213
	v_cmp_lt_i32_e32 vcc, v138, v139
	v_add_u32_e32 v167, s36, v183
	s_nop 0
	v_cndmask_b32_e32 v138, v138, v213, vcc
	s_nop 1
	v_mul_f32_e32 v142, 0x3fb8aa3b, v152
	v_exp_f32_e64 v143, -|v142|
	v_mul_f32_e32 v146, 0x3fb8aa3b, v153
	v_exp_f32_e64 v147, -|v146|
	v_lshlrev_b32_e32 v164, 2, v138
	v_add_f32_e32 v138, 1.0, v143
	v_log_f32_e32 v138, v138
	v_add_f32_e32 v143, 1.0, v147
	v_log_f32_e32 v143, v143
	v_min_f32_e32 v142, 0, v142
	v_sub_f32_e32 v138, v142, v138
	v_min_f32_e32 v142, 0, v146
	v_fma_f32 v153, v138, s40, 0
	v_mul_f32_e32 v138, 0x3fb8aa3b, v154
	v_sub_f32_e32 v142, v142, v143
	v_exp_f32_e64 v143, -|v138|
	v_mul_f32_e32 v146, 0x3fb8aa3b, v155
	v_exp_f32_e64 v147, -|v146|
	v_fmamk_f32 v152, v142, 0x3d800000, v153
	v_add_f32_e32 v142, 1.0, v143
	v_log_f32_e32 v142, v142
	v_add_f32_e32 v143, 1.0, v147
	v_log_f32_e32 v143, v143
	v_min_f32_e32 v138, 0, v138
	v_sub_f32_e32 v138, v138, v142
	v_min_f32_e32 v142, 0, v146
	v_sub_f32_e32 v142, v142, v143
	v_fmamk_f32 v155, v138, 0x3d800000, v152
	v_fmamk_f32 v154, v142, 0x3d800000, v155
	v_subrev_u32_e32 v142, 32, v213
	v_cmp_lt_i32_e32 vcc, v142, v139
	v_cndmask_b32_e32 v139, v142, v213, vcc
	v_lshlrev_b32_e32 v239, 2, v139
	v_mfma_f32_16x16x32_bf16 v[160:163], v[36:39], v[2:5], v[14:17]
	s_nop 7
	v_mul_f32_e32 v138, 0x3fb8aa3b, v160
	v_exp_f32_e64 v142, -|v138|
	v_mul_f32_e32 v139, 0x3fb8aa3b, v161
	v_exp_f32_e64 v143, -|v139|
	v_min_f32_e32 v138, 0, v138
	v_add_f32_e32 v142, 1.0, v142
	v_log_f32_e32 v142, v142
	v_add_f32_e32 v143, 1.0, v143
	v_mul_f32_e32 v150, 0x3fb8aa3b, v162
	v_log_f32_e32 v143, v143
	v_sub_f32_e32 v138, v138, v142
	v_exp_f32_e64 v151, -|v150|
	v_fma_f32 v147, v138, s40, 0
	v_mul_f32_e32 v138, 0x3fb8aa3b, v163
	v_exp_f32_e64 v142, -|v138|
	v_min_f32_e32 v139, 0, v139
	v_sub_f32_e32 v139, v139, v143
	v_fmamk_f32 v146, v139, 0x3d800000, v147
	v_add_f32_e32 v139, 1.0, v151
	v_log_f32_e32 v139, v139
	v_add_f32_e32 v142, 1.0, v142
	v_log_f32_e32 v142, v142
	v_min_f32_e32 v143, 0, v150
	v_sub_f32_e32 v139, v143, v139
	v_min_f32_e32 v138, 0, v138
	v_sub_f32_e32 v138, v138, v142
	v_fmamk_f32 v151, v139, 0x3d800000, v146
	v_fmamk_f32 v150, v138, 0x3d800000, v151
	v_mfma_f32_16x16x32_bf16 v[160:163], v[36:39], v[22:25], v[26:29]
	s_nop 7
	v_mul_f32_e32 v138, 0x3fb8aa3b, v160
	v_mul_f32_e32 v139, 0x3fb8aa3b, v161
	v_exp_f32_e64 v142, -|v138|
	v_exp_f32_e64 v143, -|v139|
	v_mul_f32_e32 v160, 0x3fb8aa3b, v162
	v_min_f32_e32 v138, 0, v138
	v_add_f32_e32 v142, 1.0, v142
	v_add_f32_e32 v143, 1.0, v143
	v_log_f32_e32 v142, v142
	v_log_f32_e32 v143, v143
	v_min_f32_e32 v139, 0, v139
	v_exp_f32_e64 v161, -|v160|
	v_sub_f32_e32 v138, v138, v142
	v_sub_f32_e32 v142, v139, v143
	v_mul_f32_e32 v143, 0x3fb8aa3b, v163
	v_exp_f32_e64 v162, -|v143|
	v_fma_f32 v139, v138, s40, 0
	v_fmamk_f32 v138, v142, 0x3d800000, v139
	v_add_f32_e32 v142, 1.0, v161
	v_log_f32_e32 v142, v142
	v_add_f32_e32 v161, 1.0, v162
	v_log_f32_e32 v161, v161
	v_min_f32_e32 v160, 0, v160
	v_sub_f32_e32 v142, v160, v142
	v_min_f32_e32 v143, 0, v143
	v_sub_f32_e32 v160, v143, v161
	v_fmamk_f32 v143, v142, 0x3d800000, v138
	v_fmamk_f32 v142, v160, 0x3d800000, v143
	v_mfma_f32_16x16x32_bf16 v[160:163], v[36:39], v[18:21], v[30:33]
	s_nop 7
	v_mul_f32_e32 v160, 0x3fb8aa3b, v160
	v_mul_f32_e32 v161, 0x3fb8aa3b, v161
	v_exp_f32_e64 v244, -|v160|
	v_exp_f32_e64 v245, -|v161|
	v_mul_f32_e32 v162, 0x3fb8aa3b, v162
	v_min_f32_e32 v160, 0, v160
	v_add_f32_e32 v244, 1.0, v244
	v_add_f32_e32 v245, 1.0, v245
	v_log_f32_e32 v244, v244
	v_log_f32_e32 v245, v245
	v_min_f32_e32 v161, 0, v161
	v_exp_f32_e64 v246, -|v162|
	v_mul_f32_e32 v163, 0x3fb8aa3b, v163
	v_sub_f32_e32 v160, v160, v244
	v_sub_f32_e32 v244, v161, v245
	v_exp_f32_e64 v245, -|v163|
	v_fma_f32 v161, v160, s40, 0
	v_fmamk_f32 v160, v244, 0x3d800000, v161
	v_add_f32_e32 v244, 1.0, v246
	v_log_f32_e32 v244, v244
	v_add_f32_e32 v245, 1.0, v245
	v_log_f32_e32 v245, v245
	v_min_f32_e32 v162, 0, v162
	v_sub_f32_e32 v162, v162, v244
	v_min_f32_e32 v163, 0, v163
	v_sub_f32_e32 v244, v163, v245
	v_fmamk_f32 v163, v162, 0x3d800000, v160
	v_fmamk_f32 v162, v244, 0x3d800000, v163
	ds_bpermute_b32 v247, v164, v154
	ds_bpermute_b32 v248, v164, v150
	ds_bpermute_b32 v249, v164, v142
	ds_bpermute_b32 v250, v164, v162
	s_waitcnt lgkmcnt(0)
	v_add_f32_e32 v247, v154, v247
	v_add_f32_e32 v248, v150, v248
	v_add_f32_e32 v249, v142, v249
	v_add_f32_e32 v250, v162, v250
	v_cndmask_b32_e64 v165, v247, v154, s[0:1]
	v_cndmask_b32_e64 v240, v248, v150, s[0:1]
	v_cndmask_b32_e64 v242, v249, v142, s[0:1]
	v_cndmask_b32_e64 v164, v250, v162, s[0:1]
	ds_bpermute_b32 v247, v239, v165
	ds_bpermute_b32 v248, v239, v240
	ds_bpermute_b32 v249, v239, v242
	ds_bpermute_b32 v250, v239, v164
	s_waitcnt lgkmcnt(0)
	v_add_f32_e32 v166, v165, v247
	v_add_f32_e32 v241, v240, v248
	v_add_f32_e32 v243, v242, v249
	v_add_f32_e32 v239, v164, v250
	s_and_saveexec_b64 s[28:29], s[10:11]
	ds_write_b32 v167, v166
	ds_write_b32 v167, v241 offset:64
	ds_write_b32 v167, v243 offset:128
	ds_write_b32 v167, v239 offset:192
	s_or_b64 exec, exec, s[28:29]
	v_cndmask_b32_e64 v167, v242, v243, s[8:9]
	v_sub_f32_e32 v242, v167, v142
	v_cndmask_b32_e64 v167, v240, v241, s[8:9]
	v_cndmask_b32_e64 v165, v165, v166, s[8:9]
	v_cndmask_b32_e64 v164, v164, v239, s[8:9]
	v_sub_f32_e32 v240, v167, v150
	v_sub_f32_e32 v166, v165, v154
	v_sub_f32_e32 v164, v164, v162
	v_pk_add_f32 v[138:139], v[138:139], v[242:243] op_sel_hi:[1,0]
	v_pk_add_f32 v[142:143], v[142:143], v[242:243] op_sel_hi:[1,0]
	v_pk_add_f32 v[146:147], v[146:147], v[240:241] op_sel_hi:[1,0]
	v_pk_add_f32 v[150:151], v[150:151], v[240:241] op_sel_hi:[1,0]
	v_pk_add_f32 v[152:153], v[152:153], v[166:167] op_sel_hi:[1,0]
	v_pk_add_f32 v[154:155], v[154:155], v[166:167] op_sel_hi:[1,0]
	v_pk_add_f32 v[160:161], v[160:161], v[164:165] op_sel_hi:[1,0]
	v_pk_add_f32 v[162:163], v[162:163], v[164:165] op_sel_hi:[1,0]

.LBB0_1172:
	s_waitcnt lgkmcnt(0)
	s_barrier
	s_cmpk_lt_i32 s39, 0x42
	s_cselect_b64 s[2:3], -1, 0
	s_cmpk_gt_i32 s39, 0x41
	s_cbranch_scc1 .LBB0_1182
	v_add_u32_e32 v132, -16, v213
	v_and_b32_e32 v136, 64, v213
	v_cmp_lt_i32_e32 vcc, v132, v136
	v_add_u32_e32 v167, s36, v187
	s_nop 0
	v_cndmask_b32_e32 v137, v132, v213, vcc
	s_waitcnt vmcnt(36)
	v_mfma_f32_16x16x32_bf16 v[132:135], v[36:39], v[6:9], v[10:13]
	v_lshlrev_b32_e32 v164, 2, v137
	s_nop 6
	v_mul_f32_e32 v132, 0x3fb8aa3b, v132
	v_exp_f32_e64 v140, -|v132|
	v_mul_f32_e32 v133, 0x3fb8aa3b, v133
	v_exp_f32_e64 v141, -|v133|
	v_min_f32_e32 v132, 0, v132
	v_add_f32_e32 v137, 1.0, v140
	v_log_f32_e32 v137, v137
	v_add_f32_e32 v140, 1.0, v141
	v_log_f32_e32 v140, v140
	v_mul_f32_e32 v135, 0x3fb8aa3b, v135
	v_sub_f32_e32 v132, v132, v137
	v_fma_f32 v145, v132, s40, 0
	v_mul_f32_e32 v132, 0x3fb8aa3b, v134
	v_exp_f32_e64 v134, -|v132|
	v_exp_f32_e64 v137, -|v135|
	v_min_f32_e32 v133, 0, v133
	v_sub_f32_e32 v133, v133, v140
	v_fmamk_f32 v144, v133, 0x3d800000, v145
	v_add_f32_e32 v133, 1.0, v134
	v_log_f32_e32 v133, v133
	v_add_f32_e32 v134, 1.0, v137
	v_log_f32_e32 v134, v134
	v_min_f32_e32 v132, 0, v132
	v_sub_f32_e32 v132, v132, v133
	v_min_f32_e32 v133, 0, v135
	v_sub_f32_e32 v133, v133, v134
	v_fmamk_f32 v149, v132, 0x3d800000, v144
	v_fmamk_f32 v148, v133, 0x3d800000, v149
	v_subrev_u32_e32 v133, 32, v213
	v_cmp_lt_i32_e32 vcc, v133, v136
	v_cndmask_b32_e32 v133, v133, v213, vcc
	v_lshlrev_b32_e32 v239, 2, v133
	v_mfma_f32_16x16x32_bf16 v[132:135], v[36:39], v[2:5], v[14:17]
	s_nop 7
	v_mul_f32_e32 v132, 0x3fb8aa3b, v132
	v_mul_f32_e32 v133, 0x3fb8aa3b, v133
	v_exp_f32_e64 v136, -|v132|
	v_exp_f32_e64 v137, -|v133|
	v_min_f32_e32 v132, 0, v132
	v_mul_f32_e32 v134, 0x3fb8aa3b, v134
	v_add_f32_e32 v136, 1.0, v136
	v_add_f32_e32 v137, 1.0, v137
	v_log_f32_e32 v136, v136
	v_log_f32_e32 v137, v137
	v_min_f32_e32 v133, 0, v133
	v_exp_f32_e64 v140, -|v134|
	v_sub_f32_e32 v132, v132, v136
	v_sub_f32_e32 v133, v133, v137
	v_fma_f32 v137, v132, s40, 0
	v_mul_f32_e32 v132, 0x3fb8aa3b, v135
	v_exp_f32_e64 v135, -|v132|
	v_fmamk_f32 v136, v133, 0x3d800000, v137
	v_add_f32_e32 v133, 1.0, v140
	v_log_f32_e32 v133, v133
	v_add_f32_e32 v135, 1.0, v135
	v_log_f32_e32 v135, v135
	v_min_f32_e32 v134, 0, v134
	v_sub_f32_e32 v133, v134, v133
	v_min_f32_e32 v132, 0, v132
	v_sub_f32_e32 v132, v132, v135
	v_fmamk_f32 v141, v133, 0x3d800000, v136
	v_fmamk_f32 v140, v132, 0x3d800000, v141
	v_mfma_f32_16x16x32_bf16 v[132:135], v[36:39], v[22:25], v[26:29]
	s_nop 7
	v_mul_f32_e32 v132, 0x3fb8aa3b, v132
	v_mul_f32_e32 v133, 0x3fb8aa3b, v133
	v_exp_f32_e64 v156, -|v132|
	v_exp_f32_e64 v157, -|v133|
	v_mul_f32_e32 v134, 0x3fb8aa3b, v134
	v_min_f32_e32 v132, 0, v132
	v_add_f32_e32 v156, 1.0, v156
	v_add_f32_e32 v157, 1.0, v157
	v_log_f32_e32 v156, v156
	v_log_f32_e32 v157, v157
	v_min_f32_e32 v133, 0, v133
	v_exp_f32_e64 v158, -|v134|
	v_mul_f32_e32 v135, 0x3fb8aa3b, v135
	v_sub_f32_e32 v132, v132, v156
	v_sub_f32_e32 v156, v133, v157
	v_exp_f32_e64 v157, -|v135|
	v_fma_f32 v133, v132, s40, 0
	v_fmamk_f32 v132, v156, 0x3d800000, v133
	v_add_f32_e32 v156, 1.0, v158
	v_log_f32_e32 v156, v156
	v_add_f32_e32 v157, 1.0, v157
	v_log_f32_e32 v157, v157
	v_min_f32_e32 v134, 0, v134
	v_sub_f32_e32 v134, v134, v156
	v_min_f32_e32 v135, 0, v135
	v_sub_f32_e32 v156, v135, v157
	v_fmamk_f32 v135, v134, 0x3d800000, v132
	v_fmamk_f32 v134, v156, 0x3d800000, v135
	v_mfma_f32_16x16x32_bf16 v[156:159], v[36:39], v[18:21], v[30:33]
	s_nop 7
	v_mul_f32_e32 v156, 0x3fb8aa3b, v156
	v_mul_f32_e32 v157, 0x3fb8aa3b, v157
	v_exp_f32_e64 v244, -|v156|
	v_exp_f32_e64 v245, -|v157|
	v_mul_f32_e32 v158, 0x3fb8aa3b, v158
	v_min_f32_e32 v156, 0, v156
	v_add_f32_e32 v244, 1.0, v244
	v_add_f32_e32 v245, 1.0, v245
	v_log_f32_e32 v244, v244
	v_log_f32_e32 v245, v245
	v_min_f32_e32 v157, 0, v157
	v_exp_f32_e64 v246, -|v158|
	v_mul_f32_e32 v159, 0x3fb8aa3b, v159
	v_sub_f32_e32 v156, v156, v244
	v_sub_f32_e32 v244, v157, v245
	v_exp_f32_e64 v245, -|v159|
	v_fma_f32 v157, v156, s40, 0
	v_fmamk_f32 v156, v244, 0x3d800000, v157
	v_add_f32_e32 v244, 1.0, v246
	v_log_f32_e32 v244, v244
	v_add_f32_e32 v245, 1.0, v245
	v_log_f32_e32 v245, v245
	v_min_f32_e32 v158, 0, v158
	v_sub_f32_e32 v158, v158, v244
	v_min_f32_e32 v159, 0, v159
	v_sub_f32_e32 v244, v159, v245
	v_fmamk_f32 v159, v158, 0x3d800000, v156
	v_fmamk_f32 v158, v244, 0x3d800000, v159
	ds_bpermute_b32 v247, v164, v148
	ds_bpermute_b32 v248, v164, v140
	ds_bpermute_b32 v249, v164, v134
	ds_bpermute_b32 v250, v164, v158
	s_waitcnt lgkmcnt(0)
	v_add_f32_e32 v247, v148, v247
	v_add_f32_e32 v248, v140, v248
	v_add_f32_e32 v249, v134, v249
	v_add_f32_e32 v250, v158, v250
	v_cndmask_b32_e64 v165, v247, v148, s[0:1]
	v_cndmask_b32_e64 v240, v248, v140, s[0:1]
	v_cndmask_b32_e64 v242, v249, v134, s[0:1]
	v_cndmask_b32_e64 v164, v250, v158, s[0:1]
	ds_bpermute_b32 v247, v239, v165
	ds_bpermute_b32 v248, v239, v240
	ds_bpermute_b32 v249, v239, v242
	ds_bpermute_b32 v250, v239, v164
	s_waitcnt lgkmcnt(0)
	v_add_f32_e32 v166, v165, v247
	v_add_f32_e32 v241, v240, v248
	v_add_f32_e32 v243, v242, v249
	v_add_f32_e32 v239, v164, v250
	s_and_saveexec_b64 s[28:29], s[10:11]
	ds_write_b32 v167, v166
	ds_write_b32 v167, v241 offset:64
	ds_write_b32 v167, v243 offset:128
	ds_write_b32 v167, v239 offset:192
	s_or_b64 exec, exec, s[28:29]
	v_cndmask_b32_e64 v167, v242, v243, s[8:9]
	v_sub_f32_e32 v242, v167, v134
	v_cndmask_b32_e64 v167, v240, v241, s[8:9]
	v_cndmask_b32_e64 v165, v165, v166, s[8:9]
	v_cndmask_b32_e64 v164, v164, v239, s[8:9]
	v_sub_f32_e32 v240, v167, v140
	v_sub_f32_e32 v166, v165, v148
	v_sub_f32_e32 v164, v164, v158
	v_pk_add_f32 v[132:133], v[132:133], v[242:243] op_sel_hi:[1,0]
	v_pk_add_f32 v[134:135], v[134:135], v[242:243] op_sel_hi:[1,0]
	v_pk_add_f32 v[136:137], v[136:137], v[240:241] op_sel_hi:[1,0]
	v_pk_add_f32 v[140:141], v[140:141], v[240:241] op_sel_hi:[1,0]
	v_pk_add_f32 v[144:145], v[144:145], v[166:167] op_sel_hi:[1,0]
	v_pk_add_f32 v[148:149], v[148:149], v[166:167] op_sel_hi:[1,0]
	v_pk_add_f32 v[156:157], v[156:157], v[164:165] op_sel_hi:[1,0]
	v_pk_add_f32 v[158:159], v[158:159], v[164:165] op_sel_hi:[1,0]
